# E36: C-unit per-wave tile loops: wait for next tile V rows + ds_write moved after this tile's compute (temps renamed off the V landing regs)
# baseline (speedup 1.0000x reference)
; template <int NH, class InitF>
; __device__ __forceinline__ void attn_core(const bf16x8 (&kf)[2][2], const LAS unsigned char* vbuf, const InitF& initf  ,
;                                           const bf16x8 (&bq)[NH][2], float (&m)[NH], float (&l)[NH], f32x4 (&O)[NH][4], int lane) {
;     bf16x8 vf[4];
;     attn_vfrag(vbuf, vf, lane);
; #pragma unroll
;     for (int hq = 0; hq < NH; ++hq) {
;         f32x4 s0 = initf(hq, 0), s1 = initf(hq, 1);
;         s0 = __builtin_amdgcn_mfma_f32_16x16x32_bf16(kf[0][0], bq[hq][0], s0, 0, 0, 0); s0 = __builtin_amdgcn_mfma_f32_16x16x32_bf16(kf[0][1], bq[hq][1], s0, 0, 0, 0);
;         s1 = __builtin_amdgcn_mfma_f32_16x16x32_bf16(kf[1][0], bq[hq][0], s1, 0, 0, 0); s1 = __builtin_amdgcn_mfma_f32_16x16x32_bf16(kf[1][1], bq[hq][1], s1, 0, 0, 0);
;         float mx = fmaxf(fmaxf(fmaxf(s0[0], s0[1]), fmaxf(s0[2], s0[3])), fmaxf(fmaxf(s1[0], s1[1]), fmaxf(s1[2], s1[3])));
;         mx = fmaxf(mx, xor_sw<16>(mx)); mx = max_x32(mx);
;         const float mn = fmaxf(m[hq], mx), corr = __builtin_amdgcn_exp2f(m[hq] - mn); m[hq] = mn;
;         float p[8], ps = 0.f;
; #pragma unroll
;         for (int i = 0; i < 8; ++i) { p[i] = __builtin_amdgcn_exp2f((i < 4 ? s0[i & 3] : s1[i & 3]) - mn); ps += p[i]; }
;         l[hq] = l[hq] * corr + ps;
;         u32x4 pw; pw.x = cvt_pk_bf16(p[0], p[1]); pw.y = cvt_pk_bf16(p[2], p[3]); pw.z = cvt_pk_bf16(p[4], p[5]); pw.w = cvt_pk_bf16(p[6], p[7]);
;         const bf16x8 pb = __builtin_bit_cast(bf16x8, pw);
;         if (__builtin_amdgcn_ballot_w64(corr != 1.0f) != 0ull) {
; #pragma unroll
;             for (int mt = 0; mt < 4; ++mt) O[hq][mt] *= corr; }
; #pragma unroll
;         for (int mt = 0; mt < 4; ++mt) O[hq][mt] = __builtin_amdgcn_mfma_f32_16x16x32_bf16(vf[mt], pb, O[hq][mt], 0, 0, 0);
;     }
; }
; template <int NH, int P, class Desc, class BiasF> ...
;     ...
;         for (int u = 0; u < U; ++u) {
;             const int t = t0 + u;
;             attn_vwrite(vr[(u + 1) % P], vl + ((u + 1) & 1) * 5120, lane);
;             const TileD td = dsc(t);
;             if (td.valid) { const LAS unsigned char* bp[NH];
; #pragma unroll
;                 for (int hq = 0; hq < NH; ++hq) bp[hq] = biasf(td, hq);
;                 auto initf = [&](int hq, int hh) { return *(const LAS f32x4*)(bp[hq] + 64 * hh); };
;                 attn_core<NH>(kf[u % P], vl + (u & 1) * 5120, initf, bq, m, l, O, lane); }
.LBB0_265:
	s_cmp_gt_i32 s33, s30
	s_cbranch_scc0 .LBB0_269
	s_lshr_b32 s16, s33, 2
	v_add_u32_e32 v32, s16, v100
	ds_read_b128 v[226:229], v32 offset:512
	s_waitcnt lgkmcnt(0)
	v_mfma_f32_16x16x32_bf16 v[40:43], v[40:43], v[0:3], v[226:229]
	s_nop 2
	ds_read_b128 v[226:229], v32 offset:576
	v_mfma_f32_16x16x32_bf16 v[230:233], v[24:27], v[4:7], v[40:43]
	s_waitcnt lgkmcnt(0)
	v_mfma_f32_16x16x32_bf16 v[34:37], v[36:39], v[0:3], v[226:229]
	v_mfma_f32_16x16x32_bf16 v[226:229], v[28:31], v[4:7], v[34:37]
	s_nop 4
	v_max_f32_e32 v24, v231, v231
	v_max_f32_e32 v25, v230, v230
	v_max_f32_e32 v26, v233, v233
	v_max_f32_e32 v27, v232, v232
	v_max_f32_e32 v24, v25, v24
	v_max_f32_e32 v28, v229, v229
	v_max_f32_e32 v29, v228, v228
	v_max_f32_e32 v25, v27, v26
	v_max_f32_e32 v26, v29, v28
	v_max3_f32 v26, v226, v227, v26
	v_max3_f32 v26, v24, v25, v26
	ds_swizzle_b32 v27, v26 offset:swizzle(SWAP,16)
	ds_read_b64_tr_b16 v[38:39], v191
	ds_read_b64_tr_b16 v[34:35], v191 offset:32
	ds_read_b64_tr_b16 v[28:29], v191 offset:64
	ds_read_b64_tr_b16 v[24:25], v191 offset:96
	s_waitcnt lgkmcnt(4)
	v_max_f32_e32 v27, v27, v27
	v_max_f32_e32 v26, v26, v27
	v_mov_b32_e32 v27, v26
	s_nop 1
	v_permlane32_swap_b32_e32 v26, v27
	v_max3_f32 v76, v116, v26, v27
	v_sub_f32_e32 v26, v116, v76
	v_exp_f32_e32 v32, v26
	ds_read_b64_tr_b16 v[40:41], v191 offset:2560
	ds_read_b64_tr_b16 v[36:37], v191 offset:2592
	ds_read_b64_tr_b16 v[30:31], v191 offset:2624
	ds_read_b64_tr_b16 v[26:27], v191 offset:2656
	v_cmp_neq_f32_e32 vcc, 1.0, v32
	s_cbranch_vccz .LBB0_268
	v_pk_mul_f32 v[22:23], v[22:23], v[32:33] op_sel_hi:[1,0]
	v_pk_mul_f32 v[20:21], v[20:21], v[32:33] op_sel_hi:[1,0]
	v_pk_mul_f32 v[18:19], v[18:19], v[32:33] op_sel_hi:[1,0]
	v_pk_mul_f32 v[16:17], v[16:17], v[32:33] op_sel_hi:[1,0]
	v_pk_mul_f32 v[14:15], v[14:15], v[32:33] op_sel_hi:[1,0]
	v_pk_mul_f32 v[12:13], v[12:13], v[32:33] op_sel_hi:[1,0]
	v_pk_mul_f32 v[10:11], v[10:11], v[32:33] op_sel_hi:[1,0]
	v_pk_mul_f32 v[8:9], v[8:9], v[32:33] op_sel_hi:[1,0]
.LBB0_268:
	v_sub_f32_e32 v42, v230, v76
	v_exp_f32_e32 v42, v42
	v_sub_f32_e32 v230, v231, v76
	v_exp_f32_e32 v230, v230
	v_sub_f32_e32 v231, v232, v76
	v_exp_f32_e32 v231, v231
	v_sub_f32_e32 v232, v233, v76
	v_exp_f32_e32 v232, v232
	v_sub_f32_e32 v226, v226, v76
	v_add_f32_e32 v43, 0, v42
	v_exp_f32_e32 v233, v226
	v_sub_f32_e32 v226, v227, v76
	v_add_f32_e32 v43, v230, v43
	v_exp_f32_e32 v234, v226
	v_sub_f32_e32 v226, v228, v76
	v_add_f32_e32 v43, v231, v43
	v_exp_f32_e32 v235, v226
	v_sub_f32_e32 v226, v229, v76
	v_add_f32_e32 v43, v232, v43
	v_exp_f32_e32 v229, v226
	v_add_f32_e32 v43, v233, v43
	v_add_f32_e32 v43, v234, v43
	v_add_f32_e32 v43, v235, v43
	v_add_f32_e32 v43, v229, v43
	v_fmac_f32_e32 v43, v119, v32
	v_cvt_pk_bf16_f32 v226, v42, v230
	v_cvt_pk_bf16_f32 v227, v231, v232
	v_cvt_pk_bf16_f32 v228, v233, v234
	v_cvt_pk_bf16_f32 v229, v235, v229
	v_mov_b32_e32 v119, v43
	s_waitcnt lgkmcnt(3)
	v_mfma_f32_16x16x32_bf16 v[20:23], v[38:41], v[226:229], v[20:23]
	s_waitcnt lgkmcnt(2)
	v_mfma_f32_16x16x32_bf16 v[16:19], v[34:37], v[226:229], v[16:19]
	s_waitcnt lgkmcnt(1)
	v_mfma_f32_16x16x32_bf16 v[12:15], v[28:31], v[226:229], v[12:15]
	s_waitcnt lgkmcnt(0)
	v_mfma_f32_16x16x32_bf16 v[8:11], v[24:27], v[226:229], v[8:11]
	s_branch .LBB0_270

; #define LAS __attribute__((address_space(3)))
; __device__ __forceinline__ void attn_load(const char* kp_base, const char* vp_base, const TileD& t_, bf16x8 (&kf)[2][2], bf16x8 (&vr)[4], int lane) {
;     const int c = lane & 15, g = lane >> 4;
;     TileD t = t_; asm volatile("" : "+s"(t.kb));
;     if (!t.valid) {
; #pragma unroll
;         for (int j = 0; j < 4; ++j) { kf[j >> 1][j & 1] = (bf16x8){0, 0, 0, 0, 0, 0, 0, 0}; vr[j] = (bf16x8){0, 0, 0, 0, 0, 0, 0, 0}; }
;         return; }
; template <int NH, int P, class Desc, class BiasF> ...
;     ...
;             attn_vwrite(vr[(u + 1) % P], vl + ((u + 1) & 1) * 5120, lane);
;             const TileD td = dsc(t);
;             if (td.valid) { const LAS unsigned char* bp[NH];
; #pragma unroll
;                 for (int hq = 0; hq < NH; ++hq) bp[hq] = biasf(td, hq);
;                 auto initf = [&](int hq, int hh) { return *(const LAS f32x4*)(bp[hq] + 64 * hh); };
;                 attn_core<NH>(kf[u % P], vl + (u & 1) * 5120, initf, bq, m, l, O, lane); }
;             attn_load(kp_base, vp_base, dsc(t + P), kf[u % P], vr[u % P], lane);
.LBB0_270:
	s_waitcnt vmcnt(3)
	ds_write_b128 v187, v[60:63] offset:5120
	s_waitcnt vmcnt(2)
	ds_write_b128 v188, v[64:67] offset:5120
	s_waitcnt vmcnt(1)
	ds_write_b128 v189, v[68:71] offset:5120
	s_waitcnt vmcnt(0)
	ds_write_b128 v190, v[72:75] offset:5120
	s_xor_b64 s[16:17], s[14:15], -1
	s_add_i32 s34, s33, 0x400
	s_cmp_lt_u32 s34, s31
	s_cselect_b64 s[18:19], -1, 0
	s_and_b64 s[40:41], s[14:15], s[18:19]
	s_add_i32 s34, s34, s73
	s_mov_b64 s[18:19], -1
	s_and_b64 vcc, exec, s[40:41]
	s_cbranch_vccnz .LBB0_272
	v_mov_b32_e32 v40, 0
	v_mov_b32_e32 v41, 0
	v_mov_b32_e32 v42, 0
	v_mov_b32_e32 v43, 0
	v_mov_b32_e32 v24, 0
	v_mov_b32_e32 v25, 0
	v_mov_b32_e32 v26, 0
	v_mov_b32_e32 v27, 0
	v_mov_b32_e32 v36, 0
	v_mov_b32_e32 v37, 0
	v_mov_b32_e32 v38, 0
	v_mov_b32_e32 v39, 0
	v_mov_b32_e32 v28, 0
	v_mov_b32_e32 v29, 0
	v_mov_b32_e32 v30, 0
	v_mov_b32_e32 v31, 0
	s_mov_b64 s[18:19], 0

; template <int NH, class InitF>
; __device__ __forceinline__ void attn_core(const bf16x8 (&kf)[2][2], const LAS unsigned char* vbuf, const InitF& initf  ,
;                                           const bf16x8 (&bq)[NH][2], float (&m)[NH], float (&l)[NH], f32x4 (&O)[NH][4], int lane) {
;     bf16x8 vf[4];
;     attn_vfrag(vbuf, vf, lane);
; #pragma unroll
;     for (int hq = 0; hq < NH; ++hq) {
;         f32x4 s0 = initf(hq, 0), s1 = initf(hq, 1);
;         s0 = __builtin_amdgcn_mfma_f32_16x16x32_bf16(kf[0][0], bq[hq][0], s0, 0, 0, 0); s0 = __builtin_amdgcn_mfma_f32_16x16x32_bf16(kf[0][1], bq[hq][1], s0, 0, 0, 0);
;         s1 = __builtin_amdgcn_mfma_f32_16x16x32_bf16(kf[1][0], bq[hq][0], s1, 0, 0, 0); s1 = __builtin_amdgcn_mfma_f32_16x16x32_bf16(kf[1][1], bq[hq][1], s1, 0, 0, 0);
;         float mx = fmaxf(fmaxf(fmaxf(s0[0], s0[1]), fmaxf(s0[2], s0[3])), fmaxf(fmaxf(s1[0], s1[1]), fmaxf(s1[2], s1[3])));
;         mx = fmaxf(mx, xor_sw<16>(mx)); mx = max_x32(mx);
;         const float mn = fmaxf(m[hq], mx), corr = __builtin_amdgcn_exp2f(m[hq] - mn); m[hq] = mn;
;         float p[8], ps = 0.f;
; #pragma unroll
;         for (int i = 0; i < 8; ++i) { p[i] = __builtin_amdgcn_exp2f((i < 4 ? s0[i & 3] : s1[i & 3]) - mn); ps += p[i]; }
;         l[hq] = l[hq] * corr + ps;
;         u32x4 pw; pw.x = cvt_pk_bf16(p[0], p[1]); pw.y = cvt_pk_bf16(p[2], p[3]); pw.z = cvt_pk_bf16(p[4], p[5]); pw.w = cvt_pk_bf16(p[6], p[7]);
;         const bf16x8 pb = __builtin_bit_cast(bf16x8, pw);
;         if (__builtin_amdgcn_ballot_w64(corr != 1.0f) != 0ull) {
; #pragma unroll
;             for (int mt = 0; mt < 4; ++mt) O[hq][mt] *= corr; }
; #pragma unroll
;         for (int mt = 0; mt < 4; ++mt) O[hq][mt] = __builtin_amdgcn_mfma_f32_16x16x32_bf16(vf[mt], pb, O[hq][mt], 0, 0, 0);
;     }
; }
; template <int NH, int P, class Desc, class BiasF> ...
;     ...
;         for (int u = 0; u < U; ++u) {
;             const int t = t0 + u;
;             attn_vwrite(vr[(u + 1) % P], vl + ((u + 1) & 1) * 5120, lane);
;             const TileD td = dsc(t);
;             if (td.valid) { const LAS unsigned char* bp[NH];
; #pragma unroll
;                 for (int hq = 0; hq < NH; ++hq) bp[hq] = biasf(td, hq);
;                 auto initf = [&](int hq, int hh) { return *(const LAS f32x4*)(bp[hq] + 64 * hh); };
;                 attn_core<NH>(kf[u % P], vl + (u & 1) * 5120, initf, bq, m, l, O, lane); }
.LBB0_275:
	s_or_b32 s18, s33, 0x200
	s_cmp_ge_u32 s18, s31
	s_cbranch_scc1 .LBB0_279
	s_lshr_b32 s18, s18, 2
	v_add_u32_e32 v32, s18, v100
	ds_read_b128 v[226:229], v32 offset:512
	s_waitcnt lgkmcnt(0)
	v_mfma_f32_16x16x32_bf16 v[56:59], v[56:59], v[0:3], v[226:229]
	s_nop 2
	ds_read_b128 v[226:229], v32 offset:576
	v_mfma_f32_16x16x32_bf16 v[230:233], v[44:47], v[4:7], v[56:59]
	s_waitcnt lgkmcnt(0)
	v_mfma_f32_16x16x32_bf16 v[48:51], v[48:51], v[0:3], v[226:229]
	v_mfma_f32_16x16x32_bf16 v[226:229], v[52:55], v[4:7], v[48:51]
	s_nop 4
	v_max_f32_e32 v32, v231, v231
	v_max_f32_e32 v34, v230, v230
	v_max_f32_e32 v35, v233, v233
	v_max_f32_e32 v44, v232, v232
	v_max_f32_e32 v32, v34, v32
	v_max_f32_e32 v45, v229, v229
	v_max_f32_e32 v46, v228, v228
	v_max_f32_e32 v34, v44, v35
	v_max_f32_e32 v35, v46, v45
	v_max3_f32 v35, v226, v227, v35
	v_max3_f32 v32, v32, v34, v35
	ds_swizzle_b32 v34, v32 offset:swizzle(SWAP,16)
	ds_read_b64_tr_b16 v[56:57], v191 offset:5120
	ds_read_b64_tr_b16 v[52:53], v191 offset:5152
	ds_read_b64_tr_b16 v[48:49], v191 offset:5184
	ds_read_b64_tr_b16 v[44:45], v191 offset:5216
	ds_read_b64_tr_b16 v[58:59], v191 offset:7680
	ds_read_b64_tr_b16 v[54:55], v191 offset:7712
	ds_read_b64_tr_b16 v[50:51], v191 offset:7744
	ds_read_b64_tr_b16 v[46:47], v191 offset:7776
	s_waitcnt lgkmcnt(8)
	v_max_f32_e32 v34, v34, v34
	v_max_f32_e32 v32, v32, v34
	v_mov_b32_e32 v34, v32
	s_nop 1
	v_permlane32_swap_b32_e32 v32, v34
	v_max3_f32 v116, v76, v32, v34
	v_sub_f32_e32 v32, v76, v116
	v_exp_f32_e32 v32, v32
	s_nop 0
	v_cmp_neq_f32_e32 vcc, 1.0, v32
	s_cbranch_vccz .LBB0_278
	v_pk_mul_f32 v[22:23], v[22:23], v[32:33] op_sel_hi:[1,0]
	v_pk_mul_f32 v[20:21], v[20:21], v[32:33] op_sel_hi:[1,0]
	v_pk_mul_f32 v[18:19], v[18:19], v[32:33] op_sel_hi:[1,0]
	v_pk_mul_f32 v[16:17], v[16:17], v[32:33] op_sel_hi:[1,0]
	v_pk_mul_f32 v[14:15], v[14:15], v[32:33] op_sel_hi:[1,0]
	v_pk_mul_f32 v[12:13], v[12:13], v[32:33] op_sel_hi:[1,0]
	v_pk_mul_f32 v[10:11], v[10:11], v[32:33] op_sel_hi:[1,0]
	v_pk_mul_f32 v[8:9], v[8:9], v[32:33] op_sel_hi:[1,0]
.LBB0_278:
	v_sub_f32_e32 v34, v230, v116
	v_exp_f32_e32 v34, v34
	v_sub_f32_e32 v230, v231, v116
	v_exp_f32_e32 v230, v230
	v_sub_f32_e32 v231, v232, v116
	v_exp_f32_e32 v231, v231
	v_sub_f32_e32 v232, v233, v116
	v_exp_f32_e32 v232, v232
	v_sub_f32_e32 v226, v226, v116
	v_add_f32_e32 v35, 0, v34
	v_exp_f32_e32 v233, v226
	v_sub_f32_e32 v226, v227, v116
	v_add_f32_e32 v35, v230, v35
	v_exp_f32_e32 v234, v226
	v_sub_f32_e32 v226, v228, v116
	v_add_f32_e32 v35, v231, v35
	v_exp_f32_e32 v235, v226
	v_sub_f32_e32 v226, v229, v116
	v_add_f32_e32 v35, v232, v35
	v_exp_f32_e32 v229, v226
	v_add_f32_e32 v35, v233, v35
	v_add_f32_e32 v35, v234, v35
	v_add_f32_e32 v35, v235, v35
	v_add_f32_e32 v35, v229, v35
	v_cvt_pk_bf16_f32 v226, v34, v230
	v_cvt_pk_bf16_f32 v227, v231, v232
	v_cvt_pk_bf16_f32 v228, v233, v234
	v_cvt_pk_bf16_f32 v229, v235, v229
	v_fmac_f32_e32 v35, v119, v32
	v_mov_b32_e32 v119, v35
	s_waitcnt lgkmcnt(3)
	v_mfma_f32_16x16x32_bf16 v[20:23], v[56:59], v[226:229], v[20:23]
	s_waitcnt lgkmcnt(2)
	v_mfma_f32_16x16x32_bf16 v[16:19], v[52:55], v[226:229], v[16:19]
	s_waitcnt lgkmcnt(1)
	v_mfma_f32_16x16x32_bf16 v[12:15], v[48:51], v[226:229], v[12:15]
	s_waitcnt lgkmcnt(0)
	v_mfma_f32_16x16x32_bf16 v[8:11], v[44:47], v[226:229], v[8:11]
	s_branch .LBB0_280

; #define LAS __attribute__((address_space(3)))
; __device__ __forceinline__ void attn_load(const char* kp_base, const char* vp_base, const TileD& t_, bf16x8 (&kf)[2][2], bf16x8 (&vr)[4], int lane) {
;     const int c = lane & 15, g = lane >> 4;
;     TileD t = t_; asm volatile("" : "+s"(t.kb));
;     if (!t.valid) {
; #pragma unroll
;         for (int j = 0; j < 4; ++j) { kf[j >> 1][j & 1] = (bf16x8){0, 0, 0, 0, 0, 0, 0, 0}; vr[j] = (bf16x8){0, 0, 0, 0, 0, 0, 0, 0}; }
;         return; }
; template <int NH, int P, class Desc, class BiasF> ...
;     ...
;             attn_vwrite(vr[(u + 1) % P], vl + ((u + 1) & 1) * 5120, lane);
;             const TileD td = dsc(t);
;             if (td.valid) { const LAS unsigned char* bp[NH];
; #pragma unroll
;                 for (int hq = 0; hq < NH; ++hq) bp[hq] = biasf(td, hq);
;                 auto initf = [&](int hq, int hh) { return *(const LAS f32x4*)(bp[hq] + 64 * hh); };
;                 attn_core<NH>(kf[u % P], vl + (u & 1) * 5120, initf, bq, m, l, O, lane); }
;             attn_load(kp_base, vp_base, dsc(t + P), kf[u % P], vr[u % P], lane);
.LBB0_280:
	s_waitcnt vmcnt(3)
	ds_write_b128 v187, v[68:71]
	s_waitcnt vmcnt(2)
	ds_write_b128 v188, v[60:63]
	s_waitcnt vmcnt(1)
	ds_write_b128 v189, v[64:67]
	s_waitcnt vmcnt(0)
	ds_write_b128 v190, v[72:75]
	s_addk_i32 s33, 0x600
	s_cmp_lt_u32 s33, s31
	s_cselect_b64 s[18:19], -1, 0
	s_and_b64 s[34:35], s[14:15], s[18:19]
	s_add_i32 s18, s33, s73
	s_mov_b64 s[14:15], -1
	s_and_b64 vcc, exec, s[34:35]
	s_cbranch_vccnz .LBB0_282
	v_mov_b32_e32 v56, 0
	v_mov_b32_e32 v57, 0
	v_mov_b32_e32 v58, 0
	v_mov_b32_e32 v59, 0
	v_mov_b32_e32 v44, 0
	v_mov_b32_e32 v45, 0
	v_mov_b32_e32 v46, 0
	v_mov_b32_e32 v47, 0
	v_mov_b32_e32 v48, 0
	v_mov_b32_e32 v49, 0
	v_mov_b32_e32 v50, 0
	v_mov_b32_e32 v51, 0
	v_mov_b32_e32 v52, 0
	v_mov_b32_e32 v53, 0
	v_mov_b32_e32 v54, 0
	s_mov_b64 s[14:15], 0
	v_mov_b32_e32 v55, 0

; template <int NH, class InitF>
; __device__ __forceinline__ void attn_core(const bf16x8 (&kf)[2][2], const LAS unsigned char* vbuf, const InitF& initf  ,
;                                           const bf16x8 (&bq)[NH][2], float (&m)[NH], float (&l)[NH], f32x4 (&O)[NH][4], int lane) {
;     bf16x8 vf[4];
;     attn_vfrag(vbuf, vf, lane);
; #pragma unroll
;     for (int hq = 0; hq < NH; ++hq) {
;         f32x4 s0 = initf(hq, 0), s1 = initf(hq, 1);
;         s0 = __builtin_amdgcn_mfma_f32_16x16x32_bf16(kf[0][0], bq[hq][0], s0, 0, 0, 0); s0 = __builtin_amdgcn_mfma_f32_16x16x32_bf16(kf[0][1], bq[hq][1], s0, 0, 0, 0);
;         s1 = __builtin_amdgcn_mfma_f32_16x16x32_bf16(kf[1][0], bq[hq][0], s1, 0, 0, 0); s1 = __builtin_amdgcn_mfma_f32_16x16x32_bf16(kf[1][1], bq[hq][1], s1, 0, 0, 0);
;         float mx = fmaxf(fmaxf(fmaxf(s0[0], s0[1]), fmaxf(s0[2], s0[3])), fmaxf(fmaxf(s1[0], s1[1]), fmaxf(s1[2], s1[3])));
;         mx = fmaxf(mx, xor_sw<16>(mx)); mx = max_x32(mx);
;         const float mn = fmaxf(m[hq], mx), corr = __builtin_amdgcn_exp2f(m[hq] - mn); m[hq] = mn;
;         float p[8], ps = 0.f;
; #pragma unroll
;         for (int i = 0; i < 8; ++i) { p[i] = __builtin_amdgcn_exp2f((i < 4 ? s0[i & 3] : s1[i & 3]) - mn); ps += p[i]; }
;         l[hq] = l[hq] * corr + ps;
;         u32x4 pw; pw.x = cvt_pk_bf16(p[0], p[1]); pw.y = cvt_pk_bf16(p[2], p[3]); pw.z = cvt_pk_bf16(p[4], p[5]); pw.w = cvt_pk_bf16(p[6], p[7]);
;         const bf16x8 pb = __builtin_bit_cast(bf16x8, pw);
;         if (__builtin_amdgcn_ballot_w64(corr != 1.0f) != 0ull) {
; #pragma unroll
;             for (int mt = 0; mt < 4; ++mt) O[hq][mt] *= corr; }
; #pragma unroll
;         for (int mt = 0; mt < 4; ++mt) O[hq][mt] = __builtin_amdgcn_mfma_f32_16x16x32_bf16(vf[mt], pb, O[hq][mt], 0, 0, 0);
;     }
; }
; template <int NH, int P, class Desc, class BiasF> ...
;     ...
;         for (int u = 0; u < U; ++u) {
;             const int t = t0 + u;
;             attn_vwrite(vr[(u + 1) % P], vl + ((u + 1) & 1) * 5120, lane);
;             const TileD td = dsc(t);
;             if (td.valid) { const LAS unsigned char* bp[NH];
; #pragma unroll
;                 for (int hq = 0; hq < NH; ++hq) bp[hq] = biasf(td, hq);
;                 auto initf = [&](int hq, int hh) { return *(const LAS f32x4*)(bp[hq] + 64 * hh); };
;                 attn_core<NH>(kf[u % P], vl + (u & 1) * 5120, initf, bq, m, l, O, lane); }
.LBB0_289:
	s_cmp_gt_i32 s16, s30
	s_cbranch_scc0 .LBB0_293
	s_lshr_b32 s12, s16, 2
	v_add_u32_e32 v32, s12, v100
	ds_read_b128 v[226:229], v32 offset:512
	s_waitcnt lgkmcnt(0)
	v_mfma_f32_16x16x32_bf16 v[64:67], v[64:67], v[24:27], v[226:229]
	s_nop 2
	ds_read_b128 v[226:229], v32 offset:576
	v_mfma_f32_16x16x32_bf16 v[230:233], v[52:55], v[28:31], v[64:67]
	s_waitcnt lgkmcnt(0)
	v_mfma_f32_16x16x32_bf16 v[60:63], v[60:63], v[24:27], v[226:229]
	v_mfma_f32_16x16x32_bf16 v[226:229], v[56:59], v[28:31], v[60:63]
	s_nop 4
	v_max_f32_e32 v32, v231, v231
	v_max_f32_e32 v34, v230, v230
	v_max_f32_e32 v35, v233, v233
	v_max_f32_e32 v52, v232, v232
	v_max_f32_e32 v32, v34, v32
	v_max_f32_e32 v53, v229, v229
	v_max_f32_e32 v54, v228, v228
	v_max_f32_e32 v34, v52, v35
	v_max_f32_e32 v35, v54, v53
	v_max3_f32 v35, v226, v227, v35
	v_max3_f32 v32, v32, v34, v35
	ds_swizzle_b32 v34, v32 offset:swizzle(SWAP,16)
	ds_read_b64_tr_b16 v[64:65], v191
	ds_read_b64_tr_b16 v[60:61], v191 offset:32
	ds_read_b64_tr_b16 v[56:57], v191 offset:64
	ds_read_b64_tr_b16 v[52:53], v191 offset:96
	ds_read_b64_tr_b16 v[66:67], v191 offset:2560
	ds_read_b64_tr_b16 v[62:63], v191 offset:2592
	ds_read_b64_tr_b16 v[58:59], v191 offset:2624
	ds_read_b64_tr_b16 v[54:55], v191 offset:2656
	s_waitcnt lgkmcnt(8)
	v_max_f32_e32 v34, v34, v34
	v_max_f32_e32 v32, v32, v34
	v_mov_b32_e32 v34, v32
	s_nop 1
	v_permlane32_swap_b32_e32 v32, v34
	v_max3_f32 v34, v118, v32, v34
	v_sub_f32_e32 v32, v118, v34
	v_exp_f32_e32 v32, v32
	s_nop 0
	v_cmp_neq_f32_e32 vcc, 1.0, v32
	s_cbranch_vccz .LBB0_292
	v_pk_mul_f32 v[50:51], v[50:51], v[32:33] op_sel_hi:[1,0]
	v_pk_mul_f32 v[48:49], v[48:49], v[32:33] op_sel_hi:[1,0]
	v_pk_mul_f32 v[46:47], v[46:47], v[32:33] op_sel_hi:[1,0]
	v_pk_mul_f32 v[44:45], v[44:45], v[32:33] op_sel_hi:[1,0]
	v_pk_mul_f32 v[42:43], v[42:43], v[32:33] op_sel_hi:[1,0]
	v_pk_mul_f32 v[40:41], v[40:41], v[32:33] op_sel_hi:[1,0]
	v_pk_mul_f32 v[38:39], v[38:39], v[32:33] op_sel_hi:[1,0]
	v_pk_mul_f32 v[36:37], v[36:37], v[32:33] op_sel_hi:[1,0]
.LBB0_292:
	v_sub_f32_e32 v35, v230, v34
	v_exp_f32_e32 v35, v35
	v_sub_f32_e32 v231, v231, v34
	v_exp_f32_e32 v231, v231
	v_sub_f32_e32 v232, v232, v34
	v_exp_f32_e32 v232, v232
	v_sub_f32_e32 v233, v233, v34
	v_exp_f32_e32 v233, v233
	v_sub_f32_e32 v226, v226, v34
	v_add_f32_e32 v230, 0, v35
	v_exp_f32_e32 v234, v226
	v_add_f32_e32 v230, v231, v230
	v_add_f32_e32 v230, v232, v230
	v_add_f32_e32 v230, v233, v230
	v_sub_f32_e32 v227, v227, v34
	v_add_f32_e32 v226, v234, v230
	v_exp_f32_e32 v230, v227
	v_sub_f32_e32 v227, v228, v34
	v_exp_f32_e32 v235, v227
	v_sub_f32_e32 v227, v229, v34
	v_exp_f32_e32 v229, v227
	v_add_f32_e32 v226, v230, v226
	v_add_f32_e32 v226, v235, v226
	v_cvt_pk_bf16_f32 v227, v232, v233
	v_add_f32_e32 v236, v229, v226
	v_fmac_f32_e32 v236, v133, v32
	v_cvt_pk_bf16_f32 v226, v35, v231
	v_cvt_pk_bf16_f32 v228, v234, v230
	v_cvt_pk_bf16_f32 v229, v235, v229
	v_mov_b32_e32 v133, v236
	s_waitcnt lgkmcnt(3)
	v_mfma_f32_16x16x32_bf16 v[48:51], v[64:67], v[226:229], v[48:51]
	s_waitcnt lgkmcnt(2)
	v_mfma_f32_16x16x32_bf16 v[44:47], v[60:63], v[226:229], v[44:47]
	s_waitcnt lgkmcnt(1)
	v_mfma_f32_16x16x32_bf16 v[40:43], v[56:59], v[226:229], v[40:43]
	s_waitcnt lgkmcnt(0)
	v_mfma_f32_16x16x32_bf16 v[36:39], v[52:55], v[226:229], v[36:39]
	s_branch .LBB0_294

; #define LAS __attribute__((address_space(3)))
; __device__ __forceinline__ void attn_load(const char* kp_base, const char* vp_base, const TileD& t_, bf16x8 (&kf)[2][2], bf16x8 (&vr)[4], int lane) {
;     const int c = lane & 15, g = lane >> 4;
;     TileD t = t_; asm volatile("" : "+s"(t.kb));
;     if (!t.valid) {
; #pragma unroll
;         for (int j = 0; j < 4; ++j) { kf[j >> 1][j & 1] = (bf16x8){0, 0, 0, 0, 0, 0, 0, 0}; vr[j] = (bf16x8){0, 0, 0, 0, 0, 0, 0, 0}; }
;         return; }
; template <int NH, int P, class Desc, class BiasF> ...
;     ...
;             attn_vwrite(vr[(u + 1) % P], vl + ((u + 1) & 1) * 5120, lane);
;             const TileD td = dsc(t);
;             if (td.valid) { const LAS unsigned char* bp[NH];
; #pragma unroll
;                 for (int hq = 0; hq < NH; ++hq) bp[hq] = biasf(td, hq);
;                 auto initf = [&](int hq, int hh) { return *(const LAS f32x4*)(bp[hq] + 64 * hh); };
;                 attn_core<NH>(kf[u % P], vl + (u & 1) * 5120, initf, bq, m, l, O, lane); }
;             attn_load(kp_base, vp_base, dsc(t + P), kf[u % P], vr[u % P], lane);
.LBB0_294:
	s_waitcnt vmcnt(3)
	ds_write_b128 v187, v[84:87] offset:5120
	s_waitcnt vmcnt(2)
	ds_write_b128 v188, v[88:91] offset:5120
	s_waitcnt vmcnt(1)
	ds_write_b128 v189, v[92:95] offset:5120
	s_waitcnt vmcnt(0)
	ds_write_b128 v190, v[96:99] offset:5120
	s_xor_b64 s[12:13], s[10:11], -1
	s_add_i32 s17, s16, 0x400
	s_cmp_lt_u32 s17, s31
	s_cselect_b64 s[14:15], -1, 0
	s_and_b64 s[18:19], s[10:11], s[14:15]
	s_add_i32 s17, s17, s78
	s_mov_b64 s[14:15], -1
	s_and_b64 vcc, exec, s[18:19]
	s_cbranch_vccnz .LBB0_296
	v_mov_b32_e32 v64, 0
	v_mov_b32_e32 v65, 0
	v_mov_b32_e32 v66, 0
	v_mov_b32_e32 v67, 0
	v_mov_b32_e32 v52, 0
	v_mov_b32_e32 v53, 0
	v_mov_b32_e32 v54, 0
	v_mov_b32_e32 v55, 0
	v_mov_b32_e32 v60, 0
	v_mov_b32_e32 v61, 0
	v_mov_b32_e32 v62, 0
	v_mov_b32_e32 v63, 0
	v_mov_b32_e32 v56, 0
	v_mov_b32_e32 v57, 0
	v_mov_b32_e32 v58, 0
	v_mov_b32_e32 v59, 0
	s_mov_b64 s[14:15], 0

; template <int NH, class InitF>
; __device__ __forceinline__ void attn_core(const bf16x8 (&kf)[2][2], const LAS unsigned char* vbuf, const InitF& initf  ,
;                                           const bf16x8 (&bq)[NH][2], float (&m)[NH], float (&l)[NH], f32x4 (&O)[NH][4], int lane) {
;     bf16x8 vf[4];
;     attn_vfrag(vbuf, vf, lane);
; #pragma unroll
;     for (int hq = 0; hq < NH; ++hq) {
;         f32x4 s0 = initf(hq, 0), s1 = initf(hq, 1);
;         s0 = __builtin_amdgcn_mfma_f32_16x16x32_bf16(kf[0][0], bq[hq][0], s0, 0, 0, 0); s0 = __builtin_amdgcn_mfma_f32_16x16x32_bf16(kf[0][1], bq[hq][1], s0, 0, 0, 0);
;         s1 = __builtin_amdgcn_mfma_f32_16x16x32_bf16(kf[1][0], bq[hq][0], s1, 0, 0, 0); s1 = __builtin_amdgcn_mfma_f32_16x16x32_bf16(kf[1][1], bq[hq][1], s1, 0, 0, 0);
;         float mx = fmaxf(fmaxf(fmaxf(s0[0], s0[1]), fmaxf(s0[2], s0[3])), fmaxf(fmaxf(s1[0], s1[1]), fmaxf(s1[2], s1[3])));
;         mx = fmaxf(mx, xor_sw<16>(mx)); mx = max_x32(mx);
;         const float mn = fmaxf(m[hq], mx), corr = __builtin_amdgcn_exp2f(m[hq] - mn); m[hq] = mn;
;         float p[8], ps = 0.f;
; #pragma unroll
;         for (int i = 0; i < 8; ++i) { p[i] = __builtin_amdgcn_exp2f((i < 4 ? s0[i & 3] : s1[i & 3]) - mn); ps += p[i]; }
;         l[hq] = l[hq] * corr + ps;
;         u32x4 pw; pw.x = cvt_pk_bf16(p[0], p[1]); pw.y = cvt_pk_bf16(p[2], p[3]); pw.z = cvt_pk_bf16(p[4], p[5]); pw.w = cvt_pk_bf16(p[6], p[7]);
;         const bf16x8 pb = __builtin_bit_cast(bf16x8, pw);
;         if (__builtin_amdgcn_ballot_w64(corr != 1.0f) != 0ull) {
; #pragma unroll
;             for (int mt = 0; mt < 4; ++mt) O[hq][mt] *= corr; }
; #pragma unroll
;         for (int mt = 0; mt < 4; ++mt) O[hq][mt] = __builtin_amdgcn_mfma_f32_16x16x32_bf16(vf[mt], pb, O[hq][mt], 0, 0, 0);
;     }
; }
; template <int NH, int P, class Desc, class BiasF> ...
;     ...
;         for (int u = 0; u < U; ++u) {
;             const int t = t0 + u;
;             attn_vwrite(vr[(u + 1) % P], vl + ((u + 1) & 1) * 5120, lane);
;             const TileD td = dsc(t);
;             if (td.valid) { const LAS unsigned char* bp[NH];
; #pragma unroll
;                 for (int hq = 0; hq < NH; ++hq) bp[hq] = biasf(td, hq);
;                 auto initf = [&](int hq, int hh) { return *(const LAS f32x4*)(bp[hq] + 64 * hh); };
;                 attn_core<NH>(kf[u % P], vl + (u & 1) * 5120, initf, bq, m, l, O, lane); }
.LBB0_299:
	s_or_b32 s14, s16, 0x200
	s_cmp_ge_u32 s14, s31
	s_cbranch_scc1 .LBB0_303
	s_lshr_b32 s14, s14, 2
	v_add_u32_e32 v32, s14, v100
	ds_read_b128 v[226:229], v32 offset:512
	s_waitcnt lgkmcnt(0)
	v_mfma_f32_16x16x32_bf16 v[80:83], v[80:83], v[24:27], v[226:229]
	s_nop 2
	ds_read_b128 v[226:229], v32 offset:576
	v_mfma_f32_16x16x32_bf16 v[230:233], v[68:71], v[28:31], v[80:83]
	s_waitcnt lgkmcnt(0)
	v_mfma_f32_16x16x32_bf16 v[72:75], v[72:75], v[24:27], v[226:229]
	v_mfma_f32_16x16x32_bf16 v[226:229], v[76:79], v[28:31], v[72:75]
	s_nop 4
	v_max_f32_e32 v32, v231, v231
	v_max_f32_e32 v35, v230, v230
	v_max_f32_e32 v68, v233, v233
	v_max_f32_e32 v69, v232, v232
	v_max_f32_e32 v32, v35, v32
	v_max_f32_e32 v70, v229, v229
	v_max_f32_e32 v71, v228, v228
	v_max_f32_e32 v35, v69, v68
	v_max_f32_e32 v68, v71, v70
	v_max3_f32 v68, v226, v227, v68
	v_max3_f32 v32, v32, v35, v68
	ds_swizzle_b32 v35, v32 offset:swizzle(SWAP,16)
	ds_read_b64_tr_b16 v[80:81], v191 offset:5120
	ds_read_b64_tr_b16 v[76:77], v191 offset:5152
	ds_read_b64_tr_b16 v[72:73], v191 offset:5184
	ds_read_b64_tr_b16 v[68:69], v191 offset:5216
	ds_read_b64_tr_b16 v[82:83], v191 offset:7680
	ds_read_b64_tr_b16 v[78:79], v191 offset:7712
	ds_read_b64_tr_b16 v[74:75], v191 offset:7744
	ds_read_b64_tr_b16 v[70:71], v191 offset:7776
	s_waitcnt lgkmcnt(8)
	v_max_f32_e32 v35, v35, v35
	v_max_f32_e32 v32, v32, v35
	v_mov_b32_e32 v35, v32
	s_nop 1
	v_permlane32_swap_b32_e32 v32, v35
	v_max3_f32 v118, v34, v32, v35
	v_sub_f32_e32 v32, v34, v118
	v_exp_f32_e32 v32, v32
	s_nop 0
	v_cmp_neq_f32_e32 vcc, 1.0, v32
	s_cbranch_vccz .LBB0_302
	v_pk_mul_f32 v[50:51], v[50:51], v[32:33] op_sel_hi:[1,0]
	v_pk_mul_f32 v[48:49], v[48:49], v[32:33] op_sel_hi:[1,0]
	v_pk_mul_f32 v[46:47], v[46:47], v[32:33] op_sel_hi:[1,0]
	v_pk_mul_f32 v[44:45], v[44:45], v[32:33] op_sel_hi:[1,0]
	v_pk_mul_f32 v[42:43], v[42:43], v[32:33] op_sel_hi:[1,0]
	v_pk_mul_f32 v[40:41], v[40:41], v[32:33] op_sel_hi:[1,0]
	v_pk_mul_f32 v[38:39], v[38:39], v[32:33] op_sel_hi:[1,0]
	v_pk_mul_f32 v[36:37], v[36:37], v[32:33] op_sel_hi:[1,0]
.LBB0_302:
	v_sub_f32_e32 v34, v230, v118
	v_exp_f32_e32 v34, v34
	v_sub_f32_e32 v230, v231, v118
	v_exp_f32_e32 v230, v230
	v_sub_f32_e32 v231, v232, v118
	v_exp_f32_e32 v231, v231
	v_sub_f32_e32 v232, v233, v118
	v_exp_f32_e32 v232, v232
	v_sub_f32_e32 v226, v226, v118
	v_add_f32_e32 v35, 0, v34
	v_exp_f32_e32 v233, v226
	v_sub_f32_e32 v226, v227, v118
	v_add_f32_e32 v35, v230, v35
	v_exp_f32_e32 v234, v226
	v_sub_f32_e32 v226, v228, v118
	v_add_f32_e32 v35, v231, v35
	v_exp_f32_e32 v235, v226
	v_sub_f32_e32 v226, v229, v118
	v_add_f32_e32 v35, v232, v35
	v_exp_f32_e32 v229, v226
	v_add_f32_e32 v35, v233, v35
	v_add_f32_e32 v35, v234, v35
	v_add_f32_e32 v35, v235, v35
	v_add_f32_e32 v35, v229, v35
	v_cvt_pk_bf16_f32 v226, v34, v230
	v_cvt_pk_bf16_f32 v227, v231, v232
	v_cvt_pk_bf16_f32 v228, v233, v234
	v_cvt_pk_bf16_f32 v229, v235, v229
	v_fmac_f32_e32 v35, v133, v32
	v_mov_b32_e32 v133, v35
	s_waitcnt lgkmcnt(3)
	v_mfma_f32_16x16x32_bf16 v[48:51], v[80:83], v[226:229], v[48:51]
	s_waitcnt lgkmcnt(2)
	v_mfma_f32_16x16x32_bf16 v[44:47], v[76:79], v[226:229], v[44:47]
	s_waitcnt lgkmcnt(1)
	v_mfma_f32_16x16x32_bf16 v[40:43], v[72:75], v[226:229], v[40:43]
	s_waitcnt lgkmcnt(0)
	v_mfma_f32_16x16x32_bf16 v[36:39], v[68:71], v[226:229], v[36:39]
	s_branch .LBB0_304

; #define LAS __attribute__((address_space(3)))
; __device__ __forceinline__ void attn_load(const char* kp_base, const char* vp_base, const TileD& t_, bf16x8 (&kf)[2][2], bf16x8 (&vr)[4], int lane) {
;     const int c = lane & 15, g = lane >> 4;
;     TileD t = t_; asm volatile("" : "+s"(t.kb));
;     if (!t.valid) {
; #pragma unroll
;         for (int j = 0; j < 4; ++j) { kf[j >> 1][j & 1] = (bf16x8){0, 0, 0, 0, 0, 0, 0, 0}; vr[j] = (bf16x8){0, 0, 0, 0, 0, 0, 0, 0}; }
;         return; }
; template <int NH, int P, class Desc, class BiasF> ...
;     ...
;             attn_vwrite(vr[(u + 1) % P], vl + ((u + 1) & 1) * 5120, lane);
;             const TileD td = dsc(t);
;             if (td.valid) { const LAS unsigned char* bp[NH];
; #pragma unroll
;                 for (int hq = 0; hq < NH; ++hq) bp[hq] = biasf(td, hq);
;                 auto initf = [&](int hq, int hh) { return *(const LAS f32x4*)(bp[hq] + 64 * hh); };
;                 attn_core<NH>(kf[u % P], vl + (u & 1) * 5120, initf, bq, m, l, O, lane); }
;             attn_load(kp_base, vp_base, dsc(t + P), kf[u % P], vr[u % P], lane);
.LBB0_304:
	s_waitcnt vmcnt(3)
	ds_write_b128 v187, v[92:95]
	s_waitcnt vmcnt(2)
	ds_write_b128 v188, v[84:87]
	s_waitcnt vmcnt(1)
	ds_write_b128 v189, v[88:91]
	s_waitcnt vmcnt(0)
	ds_write_b128 v190, v[96:99]
	s_add_i32 s18, s16, 0x600
	s_cmp_lt_u32 s18, s31
	s_cselect_b64 s[14:15], -1, 0
	s_and_b64 s[16:17], s[10:11], s[14:15]
	s_add_i32 s14, s18, s78
	s_mov_b64 s[10:11], -1
	s_and_b64 vcc, exec, s[16:17]
	s_cbranch_vccnz .LBB0_306
	v_mov_b32_e32 v80, 0
	v_mov_b32_e32 v81, 0
	v_mov_b32_e32 v82, 0
	v_mov_b32_e32 v83, 0
	v_mov_b32_e32 v68, 0
	v_mov_b32_e32 v69, 0
	v_mov_b32_e32 v70, 0
	v_mov_b32_e32 v71, 0
	v_mov_b32_e32 v72, 0
	v_mov_b32_e32 v73, 0
	v_mov_b32_e32 v74, 0
	v_mov_b32_e32 v75, 0
	v_mov_b32_e32 v76, 0
	v_mov_b32_e32 v77, 0
	v_mov_b32_e32 v78, 0
	s_mov_b64 s[10:11], 0
	v_mov_b32_e32 v79, 0

; template <int NH, class InitF>
; __device__ __forceinline__ void attn_core(const bf16x8 (&kf)[2][2], const LAS unsigned char* vbuf, const InitF& initf  ,
;                                           const bf16x8 (&bq)[NH][2], float (&m)[NH], float (&l)[NH], f32x4 (&O)[NH][4], int lane) {
;     bf16x8 vf[4];
;     attn_vfrag(vbuf, vf, lane);
; #pragma unroll
;     for (int hq = 0; hq < NH; ++hq) {
;         f32x4 s0 = initf(hq, 0), s1 = initf(hq, 1);
;         s0 = __builtin_amdgcn_mfma_f32_16x16x32_bf16(kf[0][0], bq[hq][0], s0, 0, 0, 0); s0 = __builtin_amdgcn_mfma_f32_16x16x32_bf16(kf[0][1], bq[hq][1], s0, 0, 0, 0);
;         s1 = __builtin_amdgcn_mfma_f32_16x16x32_bf16(kf[1][0], bq[hq][0], s1, 0, 0, 0); s1 = __builtin_amdgcn_mfma_f32_16x16x32_bf16(kf[1][1], bq[hq][1], s1, 0, 0, 0);
;         float mx = fmaxf(fmaxf(fmaxf(s0[0], s0[1]), fmaxf(s0[2], s0[3])), fmaxf(fmaxf(s1[0], s1[1]), fmaxf(s1[2], s1[3])));
;         mx = fmaxf(mx, xor_sw<16>(mx)); mx = max_x32(mx);
;         const float mn = fmaxf(m[hq], mx), corr = __builtin_amdgcn_exp2f(m[hq] - mn); m[hq] = mn;
;         float p[8], ps = 0.f;
; #pragma unroll
;         for (int i = 0; i < 8; ++i) { p[i] = __builtin_amdgcn_exp2f((i < 4 ? s0[i & 3] : s1[i & 3]) - mn); ps += p[i]; }
;         l[hq] = l[hq] * corr + ps;
;         u32x4 pw; pw.x = cvt_pk_bf16(p[0], p[1]); pw.y = cvt_pk_bf16(p[2], p[3]); pw.z = cvt_pk_bf16(p[4], p[5]); pw.w = cvt_pk_bf16(p[6], p[7]);
;         const bf16x8 pb = __builtin_bit_cast(bf16x8, pw);
;         if (__builtin_amdgcn_ballot_w64(corr != 1.0f) != 0ull) {
; #pragma unroll
;             for (int mt = 0; mt < 4; ++mt) O[hq][mt] *= corr; }
; #pragma unroll
;         for (int mt = 0; mt < 4; ++mt) O[hq][mt] = __builtin_amdgcn_mfma_f32_16x16x32_bf16(vf[mt], pb, O[hq][mt], 0, 0, 0);
;     }
; }
; template <int NH, int P, class Desc, class BiasF> ...
;     ...
;         for (int u = 0; u < U; ++u) {
;             const int t = t0 + u;
;             attn_vwrite(vr[(u + 1) % P], vl + ((u + 1) & 1) * 5120, lane);
;             const TileD td = dsc(t);
;             if (td.valid) { const LAS unsigned char* bp[NH];
; #pragma unroll
;                 for (int hq = 0; hq < NH; ++hq) bp[hq] = biasf(td, hq);
;                 auto initf = [&](int hq, int hh) { return *(const LAS f32x4*)(bp[hq] + 64 * hh); };
;                 attn_core<NH>(kf[u % P], vl + (u & 1) * 5120, initf, bq, m, l, O, lane); }
.LBB0_317:
	s_add_i32 s30, s18, s16
	s_add_i32 s10, s30, 0xffffff00
	s_cmpk_gt_u32 s10, 0x7ff
	v_add_u32_e32 v109, s16, v108
	s_cbranch_scc1 .LBB0_323
	v_add_u32_e32 v32, 0x229c0, v109
	ds_read_b128 v[226:229], v32
	v_add_u32_e32 v32, 0x22a00, v109
	ds_read_b128 v[230:233], v32
	s_waitcnt lgkmcnt(1)
	v_mfma_f32_16x16x32_bf16 v[226:229], v[52:55], v[0:3], v[226:229]
	s_waitcnt lgkmcnt(0)
	v_mfma_f32_16x16x32_bf16 v[230:233], v[60:63], v[0:3], v[230:233]
	v_mfma_f32_16x16x32_bf16 v[100:103], v[56:59], v[4:7], v[226:229]
	v_mfma_f32_16x16x32_bf16 v[104:107], v[64:67], v[4:7], v[230:233]
	s_nop 6
	v_max_f32_e32 v32, v101, v101
	v_max_f32_e32 v34, v100, v100
	v_max_f32_e32 v226, v103, v103
	v_max_f32_e32 v227, v102, v102
	v_max_f32_e32 v228, v107, v107
	v_max_f32_e32 v229, v106, v106
	v_max_f32_e32 v32, v34, v32
	v_max_f32_e32 v34, v227, v226
	v_max_f32_e32 v226, v229, v228
	v_max3_f32 v226, v104, v105, v226
	v_max3_f32 v32, v32, v34, v226
	ds_swizzle_b32 v34, v32 offset:swizzle(SWAP,16)
	ds_read_b64_tr_b16 v[238:239], v191
	ds_read_b64_tr_b16 v[234:235], v191 offset:32
	ds_read_b64_tr_b16 v[230:231], v191 offset:64
	ds_read_b64_tr_b16 v[226:227], v191 offset:96
	ds_read_b64_tr_b16 v[240:241], v191 offset:2560
	ds_read_b64_tr_b16 v[236:237], v191 offset:2592
	ds_read_b64_tr_b16 v[232:233], v191 offset:2624
	ds_read_b64_tr_b16 v[228:229], v191 offset:2656
	s_waitcnt lgkmcnt(8)
	v_max_f32_e32 v34, v34, v34
	v_max_f32_e32 v32, v32, v34
	v_mov_b32_e32 v34, v32
	s_nop 1
	v_permlane32_swap_b32_e32 v32, v34
	v_max3_f32 v110, v116, v32, v34
	v_sub_f32_e32 v32, v116, v110
	v_exp_f32_e32 v32, v32
	s_nop 0
	v_cmp_neq_f32_e32 vcc, 1.0, v32
	s_cbranch_vccz .LBB0_320
	v_pk_mul_f32 v[22:23], v[22:23], v[32:33] op_sel_hi:[1,0]
	v_pk_mul_f32 v[20:21], v[20:21], v[32:33] op_sel_hi:[1,0]
	v_pk_mul_f32 v[18:19], v[32:33], v[18:19] op_sel_hi:[0,1]
	v_pk_mul_f32 v[16:17], v[32:33], v[16:17] op_sel_hi:[0,1]
	v_pk_mul_f32 v[14:15], v[32:33], v[14:15] op_sel_hi:[0,1]
	v_pk_mul_f32 v[12:13], v[32:33], v[12:13] op_sel_hi:[0,1]
	v_pk_mul_f32 v[10:11], v[32:33], v[10:11] op_sel_hi:[0,1]
	v_pk_mul_f32 v[8:9], v[32:33], v[8:9] op_sel_hi:[0,1]
.LBB0_320:
	v_sub_f32_e32 v100, v100, v110
	v_sub_f32_e32 v101, v101, v110
	v_sub_f32_e32 v102, v102, v110
	v_sub_f32_e32 v103, v103, v110
	v_sub_f32_e32 v104, v104, v110
	v_sub_f32_e32 v105, v105, v110
	v_sub_f32_e32 v106, v106, v110
	v_sub_f32_e32 v107, v107, v110
	v_exp_f32_e32 v100, v100
	v_exp_f32_e32 v101, v101
	v_exp_f32_e32 v102, v102
	v_exp_f32_e32 v103, v103
	v_exp_f32_e32 v104, v104
	v_exp_f32_e32 v105, v105
	v_exp_f32_e32 v106, v106
	v_exp_f32_e32 v107, v107
	v_add_u32_e32 v34, s16, v35
	v_add_u32_e32 v111, 0x229b8, v34
	v_cvt_pk_bf16_f32 v112, v100, v101
	v_cvt_pk_bf16_f32 v113, v102, v103
	v_cvt_pk_bf16_f32 v114, v104, v105
	v_cvt_pk_bf16_f32 v115, v106, v107
	v_add_u32_e32 v34, 0x229f8, v34
	ds_read_b128 v[134:137], v34
	s_waitcnt lgkmcnt(4)
	v_mfma_f32_16x16x32_bf16 v[20:23], v[238:241], v[112:115], v[20:23]
	s_waitcnt lgkmcnt(3)
	v_mfma_f32_16x16x32_bf16 v[16:19], v[234:237], v[112:115], v[16:19]
	s_waitcnt lgkmcnt(2)
	v_mfma_f32_16x16x32_bf16 v[12:15], v[230:233], v[112:115], v[12:15]
	s_waitcnt lgkmcnt(1)
	v_mfma_f32_16x16x32_bf16 v[8:11], v[226:229], v[112:115], v[8:11]
	ds_read_b128 v[112:115], v111
	s_waitcnt lgkmcnt(0)
	v_mfma_f32_16x16x32_bf16 v[52:55], v[52:55], v[24:27], v[112:115]
	v_mfma_f32_16x16x32_bf16 v[56:59], v[56:59], v[28:31], v[52:55]
	v_mfma_f32_16x16x32_bf16 v[52:55], v[60:63], v[24:27], v[134:137]
	v_mfma_f32_16x16x32_bf16 v[52:55], v[64:67], v[28:31], v[52:55]
	s_nop 5
	v_max_f32_e32 v34, v57, v57
	v_max_f32_e32 v60, v56, v56
	v_max_f32_e32 v34, v60, v34
	v_max_f32_e32 v60, v59, v59
	v_max_f32_e32 v61, v58, v58
	v_max_f32_e32 v60, v61, v60
	v_max_f32_e32 v61, v55, v55
	v_max_f32_e32 v62, v54, v54
	v_max_f32_e32 v61, v62, v61
	v_max3_f32 v61, v52, v53, v61
	v_max3_f32 v34, v34, v60, v61
	ds_swizzle_b32 v60, v34 offset:swizzle(SWAP,16)
	s_waitcnt lgkmcnt(0)
	v_max_f32_e32 v60, v60, v60
	v_max_f32_e32 v34, v34, v60
	v_mov_b32_e32 v60, v34
	s_nop 1
	v_permlane32_swap_b32_e32 v34, v60
	v_max3_f32 v111, v118, v34, v60
	v_sub_f32_e32 v34, v118, v111
	v_exp_f32_e32 v34, v34
	s_nop 0
	v_cmp_neq_f32_e32 vcc, 1.0, v34
	s_cbranch_vccz .LBB0_322
	v_pk_mul_f32 v[50:51], v[34:35], v[50:51] op_sel_hi:[0,1]
	v_pk_mul_f32 v[48:49], v[34:35], v[48:49] op_sel_hi:[0,1]
	v_pk_mul_f32 v[46:47], v[34:35], v[46:47] op_sel_hi:[0,1]
	v_pk_mul_f32 v[44:45], v[34:35], v[44:45] op_sel_hi:[0,1]
	v_pk_mul_f32 v[42:43], v[34:35], v[42:43] op_sel_hi:[0,1]
	v_pk_mul_f32 v[40:41], v[34:35], v[40:41] op_sel_hi:[0,1]
	v_pk_mul_f32 v[38:39], v[34:35], v[38:39] op_sel_hi:[0,1]
	v_pk_mul_f32 v[36:37], v[34:35], v[36:37] op_sel_hi:[0,1]
.LBB0_322:
	v_sub_f32_e32 v56, v56, v111
	v_exp_f32_e32 v56, v56
	v_sub_f32_e32 v57, v57, v111
	v_exp_f32_e32 v57, v57
	v_sub_f32_e32 v58, v58, v111
	v_exp_f32_e32 v58, v58
	v_sub_f32_e32 v59, v59, v111
	v_exp_f32_e32 v59, v59
	v_sub_f32_e32 v52, v52, v111
	v_add_f32_e32 v60, 0, v56
	v_exp_f32_e32 v61, v52
	v_sub_f32_e32 v52, v53, v111
	v_add_f32_e32 v60, v57, v60
	v_exp_f32_e32 v62, v52
	v_sub_f32_e32 v52, v54, v111
	v_add_f32_e32 v60, v58, v60
	v_exp_f32_e32 v63, v52
	v_sub_f32_e32 v52, v55, v111
	v_add_f32_e32 v60, v59, v60
	v_exp_f32_e32 v55, v52
	v_add_f32_e32 v52, v61, v60
	v_add_f32_e32 v52, v62, v52
	v_add_f32_e32 v52, v63, v52
	v_add_f32_e32 v60, v55, v52
	v_fmac_f32_e32 v60, v133, v34
	v_add_f32_e32 v34, 0, v100
	v_add_f32_e32 v34, v101, v34
	v_add_f32_e32 v34, v102, v34
	v_add_f32_e32 v34, v103, v34
	v_add_f32_e32 v34, v104, v34
	v_cvt_pk_bf16_f32 v52, v56, v57
	v_cvt_pk_bf16_f32 v53, v58, v59
	v_cvt_pk_bf16_f32 v54, v61, v62
	v_cvt_pk_bf16_f32 v55, v63, v55
	v_add_f32_e32 v34, v105, v34
	v_add_f32_e32 v34, v106, v34
	v_mfma_f32_16x16x32_bf16 v[48:51], v[238:241], v[52:55], v[48:51]
	v_add_f32_e32 v34, v107, v34
	v_fmac_f32_e32 v34, v119, v32
	v_mov_b32_e32 v119, v34
	v_mfma_f32_16x16x32_bf16 v[44:47], v[234:237], v[52:55], v[44:47]
	v_mov_b32_e32 v133, v60
	v_mfma_f32_16x16x32_bf16 v[40:43], v[230:233], v[52:55], v[40:43]
	v_mfma_f32_16x16x32_bf16 v[36:39], v[226:229], v[52:55], v[36:39]
	s_branch .LBB0_324

; #define LAS __attribute__((address_space(3)))
; __device__ __forceinline__ void attn_load(const char* kp_base, const char* vp_base, const TileD& t_, bf16x8 (&kf)[2][2], bf16x8 (&vr)[4], int lane) {
;     const int c = lane & 15, g = lane >> 4;
;     TileD t = t_; asm volatile("" : "+s"(t.kb));
;     if (!t.valid) {
; #pragma unroll
;         for (int j = 0; j < 4; ++j) { kf[j >> 1][j & 1] = (bf16x8){0, 0, 0, 0, 0, 0, 0, 0}; vr[j] = (bf16x8){0, 0, 0, 0, 0, 0, 0, 0}; }
;         return; }
; template <int NH, int P, class Desc, class BiasF> ...
;     ...
;             attn_vwrite(vr[(u + 1) % P], vl + ((u + 1) & 1) * 5120, lane);
;             const TileD td = dsc(t);
;             if (td.valid) { const LAS unsigned char* bp[NH];
; #pragma unroll
;                 for (int hq = 0; hq < NH; ++hq) bp[hq] = biasf(td, hq);
;                 auto initf = [&](int hq, int hh) { return *(const LAS f32x4*)(bp[hq] + 64 * hh); };
;                 attn_core<NH>(kf[u % P], vl + (u & 1) * 5120, initf, bq, m, l, O, lane); }
;             attn_load(kp_base, vp_base, dsc(t + P), kf[u % P], vr[u % P], lane);
.LBB0_324:
	s_waitcnt vmcnt(3)
	ds_write_b128 v187, v[92:95] offset:5120
	s_waitcnt vmcnt(2)
	ds_write_b128 v188, v[84:87] offset:5120
	s_waitcnt vmcnt(1)
	ds_write_b128 v189, v[88:91] offset:5120
	s_waitcnt vmcnt(0)
	ds_write_b128 v190, v[96:99] offset:5120
	s_cmp_lt_u32 s19, 4
	s_cselect_b64 s[12:13], -1, 0
	s_cmp_gt_u32 s19, 3
	s_cselect_b64 s[10:11], -1, 0
	s_cmpk_lt_u32 s30, 0x800
	s_cselect_b64 s[14:15], -1, 0
	s_and_b64 s[34:35], s[12:13], s[14:15]
	s_mov_b32 s31, s30
	s_mov_b64 s[14:15], -1
	s_and_b64 vcc, exec, s[34:35]
	s_cbranch_vccnz .LBB0_326
	v_mov_b32_e32 v52, 0
	v_mov_b32_e32 v53, 0
	v_mov_b32_e32 v54, 0
	v_mov_b32_e32 v55, 0
	v_mov_b32_e32 v56, 0
	v_mov_b32_e32 v57, 0
	v_mov_b32_e32 v58, 0
	v_mov_b32_e32 v59, 0
	v_mov_b32_e32 v60, 0
	v_mov_b32_e32 v61, 0
	v_mov_b32_e32 v62, 0
	v_mov_b32_e32 v63, 0
	v_mov_b32_e32 v64, 0
	v_mov_b32_e32 v65, 0
	v_mov_b32_e32 v66, 0
	v_mov_b32_e32 v67, 0
	s_mov_b64 s[14:15], 0

; template <int NH, class InitF>
; __device__ __forceinline__ void attn_core(const bf16x8 (&kf)[2][2], const LAS unsigned char* vbuf, const InitF& initf  ,
;                                           const bf16x8 (&bq)[NH][2], float (&m)[NH], float (&l)[NH], f32x4 (&O)[NH][4], int lane) {
;     bf16x8 vf[4];
;     attn_vfrag(vbuf, vf, lane);
; #pragma unroll
;     for (int hq = 0; hq < NH; ++hq) {
;         f32x4 s0 = initf(hq, 0), s1 = initf(hq, 1);
;         s0 = __builtin_amdgcn_mfma_f32_16x16x32_bf16(kf[0][0], bq[hq][0], s0, 0, 0, 0); s0 = __builtin_amdgcn_mfma_f32_16x16x32_bf16(kf[0][1], bq[hq][1], s0, 0, 0, 0);
;         s1 = __builtin_amdgcn_mfma_f32_16x16x32_bf16(kf[1][0], bq[hq][0], s1, 0, 0, 0); s1 = __builtin_amdgcn_mfma_f32_16x16x32_bf16(kf[1][1], bq[hq][1], s1, 0, 0, 0);
;         float mx = fmaxf(fmaxf(fmaxf(s0[0], s0[1]), fmaxf(s0[2], s0[3])), fmaxf(fmaxf(s1[0], s1[1]), fmaxf(s1[2], s1[3])));
;         mx = fmaxf(mx, xor_sw<16>(mx)); mx = max_x32(mx);
;         const float mn = fmaxf(m[hq], mx), corr = __builtin_amdgcn_exp2f(m[hq] - mn); m[hq] = mn;
;         float p[8], ps = 0.f;
; #pragma unroll
;         for (int i = 0; i < 8; ++i) { p[i] = __builtin_amdgcn_exp2f((i < 4 ? s0[i & 3] : s1[i & 3]) - mn); ps += p[i]; }
;         l[hq] = l[hq] * corr + ps;
;         u32x4 pw; pw.x = cvt_pk_bf16(p[0], p[1]); pw.y = cvt_pk_bf16(p[2], p[3]); pw.z = cvt_pk_bf16(p[4], p[5]); pw.w = cvt_pk_bf16(p[6], p[7]);
;         const bf16x8 pb = __builtin_bit_cast(bf16x8, pw);
;         if (__builtin_amdgcn_ballot_w64(corr != 1.0f) != 0ull) {
; #pragma unroll
;             for (int mt = 0; mt < 4; ++mt) O[hq][mt] *= corr; }
; #pragma unroll
;         for (int mt = 0; mt < 4; ++mt) O[hq][mt] = __builtin_amdgcn_mfma_f32_16x16x32_bf16(vf[mt], pb, O[hq][mt], 0, 0, 0);
;     }
; }
; template <int NH, int P, class Desc, class BiasF> ...
;     ...
;         for (int u = 0; u < U; ++u) {
;             const int t = t0 + u;
;             attn_vwrite(vr[(u + 1) % P], vl + ((u + 1) & 1) * 5120, lane);
;             const TileD td = dsc(t);
;             if (td.valid) { const LAS unsigned char* bp[NH];
; #pragma unroll
;                 for (int hq = 0; hq < NH; ++hq) bp[hq] = biasf(td, hq);
;                 auto initf = [&](int hq, int hh) { return *(const LAS f32x4*)(bp[hq] + 64 * hh); };
;                 attn_core<NH>(kf[u % P], vl + (u & 1) * 5120, initf, bq, m, l, O, lane); }
.LBB0_329:
	s_add_i32 s14, s30, 0xffffff80
	s_cmpk_gt_u32 s14, 0x7ff
	s_cbranch_scc1 .LBB0_335
	v_add_u32_e32 v32, 0x22a40, v109
	ds_read_b128 v[226:229], v32
	v_add_u32_e32 v32, 0x22a80, v109
	ds_read_b128 v[230:233], v32
	s_waitcnt lgkmcnt(1)
	v_mfma_f32_16x16x32_bf16 v[226:229], v[72:75], v[0:3], v[226:229]
	s_waitcnt lgkmcnt(0)
	v_mfma_f32_16x16x32_bf16 v[230:233], v[76:79], v[0:3], v[230:233]
	v_mfma_f32_16x16x32_bf16 v[100:103], v[68:71], v[4:7], v[226:229]
	v_mfma_f32_16x16x32_bf16 v[104:107], v[80:83], v[4:7], v[230:233]
	s_nop 6
	v_max_f32_e32 v32, v101, v101
	v_max_f32_e32 v34, v100, v100
	v_max_f32_e32 v226, v103, v103
	v_max_f32_e32 v227, v102, v102
	v_max_f32_e32 v228, v107, v107
	v_max_f32_e32 v229, v106, v106
	v_max_f32_e32 v32, v34, v32
	v_max_f32_e32 v34, v227, v226
	v_max_f32_e32 v226, v229, v228
	v_max3_f32 v226, v104, v105, v226
	v_max3_f32 v32, v32, v34, v226
	ds_swizzle_b32 v34, v32 offset:swizzle(SWAP,16)
	ds_read_b64_tr_b16 v[238:239], v191 offset:5120
	ds_read_b64_tr_b16 v[234:235], v191 offset:5152
	ds_read_b64_tr_b16 v[230:231], v191 offset:5184
	ds_read_b64_tr_b16 v[226:227], v191 offset:5216
	ds_read_b64_tr_b16 v[240:241], v191 offset:7680
	ds_read_b64_tr_b16 v[236:237], v191 offset:7712
	ds_read_b64_tr_b16 v[232:233], v191 offset:7744
	ds_read_b64_tr_b16 v[228:229], v191 offset:7776
	s_waitcnt lgkmcnt(8)
	v_max_f32_e32 v34, v34, v34
	v_max_f32_e32 v32, v32, v34
	v_mov_b32_e32 v34, v32
	s_nop 1
	v_permlane32_swap_b32_e32 v32, v34
	v_max3_f32 v116, v110, v32, v34
	v_sub_f32_e32 v32, v110, v116
	v_exp_f32_e32 v32, v32
	s_nop 0
	v_cmp_neq_f32_e32 vcc, 1.0, v32
	s_cbranch_vccz .LBB0_332
	v_pk_mul_f32 v[22:23], v[22:23], v[32:33] op_sel_hi:[1,0]
	v_pk_mul_f32 v[20:21], v[20:21], v[32:33] op_sel_hi:[1,0]
	v_pk_mul_f32 v[18:19], v[32:33], v[18:19] op_sel_hi:[0,1]
	v_pk_mul_f32 v[16:17], v[32:33], v[16:17] op_sel_hi:[0,1]
	v_pk_mul_f32 v[14:15], v[32:33], v[14:15] op_sel_hi:[0,1]
	v_pk_mul_f32 v[12:13], v[32:33], v[12:13] op_sel_hi:[0,1]
	v_pk_mul_f32 v[10:11], v[32:33], v[10:11] op_sel_hi:[0,1]
	v_pk_mul_f32 v[8:9], v[32:33], v[8:9] op_sel_hi:[0,1]
.LBB0_332:
	v_sub_f32_e32 v100, v100, v116
	v_sub_f32_e32 v101, v101, v116
	v_sub_f32_e32 v102, v102, v116
	v_sub_f32_e32 v103, v103, v116
	v_sub_f32_e32 v104, v104, v116
	v_sub_f32_e32 v105, v105, v116
	v_sub_f32_e32 v106, v106, v116
	v_sub_f32_e32 v107, v107, v116
	v_exp_f32_e32 v100, v100
	v_exp_f32_e32 v101, v101
	v_exp_f32_e32 v102, v102
	v_exp_f32_e32 v103, v103
	v_exp_f32_e32 v104, v104
	v_exp_f32_e32 v105, v105
	v_exp_f32_e32 v106, v106
	v_exp_f32_e32 v107, v107
	v_add_u32_e32 v34, s16, v35
	v_add_u32_e32 v109, 0x22a38, v34
	v_cvt_pk_bf16_f32 v112, v100, v101
	v_cvt_pk_bf16_f32 v113, v102, v103
	v_cvt_pk_bf16_f32 v114, v104, v105
	v_cvt_pk_bf16_f32 v115, v106, v107
	v_add_u32_e32 v34, 0x22a78, v34
	ds_read_b128 v[134:137], v34
	s_waitcnt lgkmcnt(4)
	v_mfma_f32_16x16x32_bf16 v[20:23], v[238:241], v[112:115], v[20:23]
	s_waitcnt lgkmcnt(3)
	v_mfma_f32_16x16x32_bf16 v[16:19], v[234:237], v[112:115], v[16:19]
	s_waitcnt lgkmcnt(2)
	v_mfma_f32_16x16x32_bf16 v[12:15], v[230:233], v[112:115], v[12:15]
	s_waitcnt lgkmcnt(1)
	v_mfma_f32_16x16x32_bf16 v[8:11], v[226:229], v[112:115], v[8:11]
	ds_read_b128 v[112:115], v109
	s_waitcnt lgkmcnt(0)
	v_mfma_f32_16x16x32_bf16 v[72:75], v[72:75], v[24:27], v[112:115]
	v_mfma_f32_16x16x32_bf16 v[72:75], v[68:71], v[28:31], v[72:75]
	v_mfma_f32_16x16x32_bf16 v[68:71], v[76:79], v[24:27], v[134:137]
	v_mfma_f32_16x16x32_bf16 v[68:71], v[80:83], v[28:31], v[68:71]
	s_nop 5
	v_max_f32_e32 v34, v73, v73
	v_max_f32_e32 v76, v72, v72
	v_max_f32_e32 v34, v76, v34
	v_max_f32_e32 v76, v75, v75
	v_max_f32_e32 v77, v74, v74
	v_max_f32_e32 v76, v77, v76
	v_max_f32_e32 v77, v71, v71
	v_max_f32_e32 v78, v70, v70
	v_max_f32_e32 v77, v78, v77
	v_max3_f32 v77, v68, v69, v77
	v_max3_f32 v34, v34, v76, v77
	ds_swizzle_b32 v76, v34 offset:swizzle(SWAP,16)
	s_waitcnt lgkmcnt(0)
	v_max_f32_e32 v76, v76, v76
	v_max_f32_e32 v34, v34, v76
	v_mov_b32_e32 v76, v34
	s_nop 1
	v_permlane32_swap_b32_e32 v34, v76
	v_max3_f32 v118, v111, v34, v76
	v_sub_f32_e32 v34, v111, v118
	v_exp_f32_e32 v34, v34
	s_nop 0
	v_cmp_neq_f32_e32 vcc, 1.0, v34
	s_cbranch_vccz .LBB0_334
	v_pk_mul_f32 v[50:51], v[34:35], v[50:51] op_sel_hi:[0,1]
	v_pk_mul_f32 v[48:49], v[34:35], v[48:49] op_sel_hi:[0,1]
	v_pk_mul_f32 v[46:47], v[34:35], v[46:47] op_sel_hi:[0,1]
	v_pk_mul_f32 v[44:45], v[34:35], v[44:45] op_sel_hi:[0,1]
	v_pk_mul_f32 v[42:43], v[34:35], v[42:43] op_sel_hi:[0,1]
	v_pk_mul_f32 v[40:41], v[34:35], v[40:41] op_sel_hi:[0,1]
	v_pk_mul_f32 v[38:39], v[34:35], v[38:39] op_sel_hi:[0,1]
	v_pk_mul_f32 v[36:37], v[34:35], v[36:37] op_sel_hi:[0,1]
.LBB0_334:
	v_sub_f32_e32 v72, v72, v118
	v_exp_f32_e32 v72, v72
	v_sub_f32_e32 v73, v73, v118
	v_exp_f32_e32 v73, v73
	v_sub_f32_e32 v74, v74, v118
	v_exp_f32_e32 v74, v74
	v_sub_f32_e32 v75, v75, v118
	v_exp_f32_e32 v75, v75
	v_sub_f32_e32 v68, v68, v118
	v_add_f32_e32 v76, 0, v72
	v_exp_f32_e32 v77, v68
	v_sub_f32_e32 v68, v69, v118
	v_add_f32_e32 v76, v73, v76
	v_exp_f32_e32 v78, v68
	v_sub_f32_e32 v68, v70, v118
	v_add_f32_e32 v76, v74, v76
	v_exp_f32_e32 v79, v68
	v_sub_f32_e32 v68, v71, v118
	v_add_f32_e32 v76, v75, v76
	v_exp_f32_e32 v71, v68
	v_add_f32_e32 v68, v77, v76
	v_add_f32_e32 v68, v78, v68
	v_add_f32_e32 v68, v79, v68
	v_add_f32_e32 v76, v71, v68
	v_fmac_f32_e32 v76, v133, v34
	v_add_f32_e32 v34, 0, v100
	v_add_f32_e32 v34, v101, v34
	v_add_f32_e32 v34, v102, v34
	v_add_f32_e32 v34, v103, v34
	v_add_f32_e32 v34, v104, v34
	v_cvt_pk_bf16_f32 v68, v72, v73
	v_cvt_pk_bf16_f32 v69, v74, v75
	v_cvt_pk_bf16_f32 v70, v77, v78
	v_cvt_pk_bf16_f32 v71, v79, v71
	v_add_f32_e32 v34, v105, v34
	v_add_f32_e32 v34, v106, v34
	v_mfma_f32_16x16x32_bf16 v[48:51], v[238:241], v[68:71], v[48:51]
	v_add_f32_e32 v34, v107, v34
	v_fmac_f32_e32 v34, v119, v32
	v_mov_b32_e32 v119, v34
	v_mfma_f32_16x16x32_bf16 v[44:47], v[234:237], v[68:71], v[44:47]
	v_mov_b32_e32 v133, v76
	v_mfma_f32_16x16x32_bf16 v[40:43], v[230:233], v[68:71], v[40:43]
	v_mfma_f32_16x16x32_bf16 v[36:39], v[226:229], v[68:71], v[36:39]
	s_branch .LBB0_336

; #define LAS __attribute__((address_space(3)))
; __device__ __forceinline__ void attn_load(const char* kp_base, const char* vp_base, const TileD& t_, bf16x8 (&kf)[2][2], bf16x8 (&vr)[4], int lane) {
;     const int c = lane & 15, g = lane >> 4;
;     TileD t = t_; asm volatile("" : "+s"(t.kb));
;     if (!t.valid) {
; #pragma unroll
;         for (int j = 0; j < 4; ++j) { kf[j >> 1][j & 1] = (bf16x8){0, 0, 0, 0, 0, 0, 0, 0}; vr[j] = (bf16x8){0, 0, 0, 0, 0, 0, 0, 0}; }
;         return; }
; template <int NH, int P, class Desc, class BiasF> ...
;     ...
;             attn_vwrite(vr[(u + 1) % P], vl + ((u + 1) & 1) * 5120, lane);
;             const TileD td = dsc(t);
;             if (td.valid) { const LAS unsigned char* bp[NH];
; #pragma unroll
;                 for (int hq = 0; hq < NH; ++hq) bp[hq] = biasf(td, hq);
;                 auto initf = [&](int hq, int hh) { return *(const LAS f32x4*)(bp[hq] + 64 * hh); };
;                 attn_core<NH>(kf[u % P], vl + (u & 1) * 5120, initf, bq, m, l, O, lane); }
;             attn_load(kp_base, vp_base, dsc(t + P), kf[u % P], vr[u % P], lane);
.LBB0_336:
	s_waitcnt vmcnt(3)
	ds_write_b128 v187, v[92:95]
	s_waitcnt vmcnt(2)
	ds_write_b128 v188, v[84:87]
	s_waitcnt vmcnt(1)
	ds_write_b128 v189, v[88:91]
	s_waitcnt vmcnt(0)
	ds_write_b128 v190, v[96:99]
	s_add_i32 s14, s30, 0x80
	s_cmpk_lt_u32 s14, 0x800
	s_cselect_b64 s[30:31], -1, 0
	s_and_b64 s[30:31], s[12:13], s[30:31]
	s_mov_b64 s[12:13], -1
	s_and_b64 vcc, exec, s[30:31]
	s_cbranch_vccnz .LBB0_338
	v_mov_b32_e32 v72, 0
	v_mov_b32_e32 v73, 0
	v_mov_b32_e32 v74, 0
	v_mov_b32_e32 v75, 0
	v_mov_b32_e32 v68, 0
	v_mov_b32_e32 v69, 0
	v_mov_b32_e32 v70, 0
	v_mov_b32_e32 v71, 0
	v_mov_b32_e32 v76, 0
	v_mov_b32_e32 v77, 0
	v_mov_b32_e32 v78, 0
	v_mov_b32_e32 v79, 0
	v_mov_b32_e32 v80, 0
	v_mov_b32_e32 v81, 0
	v_mov_b32_e32 v82, 0
	s_mov_b64 s[12:13], 0
	v_mov_b32_e32 v83, 0
